# XCD-aware bucket/chunk remaps in csr and prep; gemm tiles rebalanced so every workgroup runs 1.5 rounds; w1[3] wait moved to its MFMA
# speedup vs baseline: 1.0625x; 1.0393x over previous
.LBB0_24:
	s_andn2_b64 vcc, exec, s[4:5]
	s_mov_b32 s9, 1
	s_cbranch_vccnz .LBB0_135
	s_and_b32 s10, s2, 7
	s_lshr_b32 s2, s2, 3
	s_lshl_b32 s10, s10, 5
	s_or_b32 s2, s2, s10
	s_load_dwordx2 s[6:7], s[0:1], 0x58
	s_load_dwordx2 s[4:5], s[0:1], 0x0
	s_load_dwordx4 s[28:31], s[0:1], 0x28
	v_lshlrev_b32_e32 v12, 2, v0
	s_mov_b32 s8, 0
	v_add_u32_e32 v1, 0x30e0, v12
	s_mov_b64 s[0:1], 0
	v_mov_b32_e32 v2, 0
	s_mov_b32 s10, s8
	s_branch .LBB0_27

_Z10k_csr_agg1PKjPKiPiPtPjPK15HIP_vector_typeIjLj2EEPS7_SA_:
	s_and_b32 s3, s2, 7
	s_lshr_b32 s2, s2, 3
	s_mul_i32 s4, s3, 0x62
	s_add_i32 s3, s3, 1
	s_lshr_b32 s3, s3, 3
	s_add_i32 s2, s2, s4
	s_sub_i32 s2, s2, s3
	s_movk_i32 s3, 0x100
	v_cmp_gt_u32_e32 vcc, s3, v0
	v_mov_b32_e32 v12, 0
	v_mov_b32_e32 v14, 0
	s_and_saveexec_b64 s[4:5], vcc
	s_cbranch_execz .LBB1_2
	s_load_dwordx2 s[6:7], s[0:1], 0x8
	s_lshl_b32 s3, s2, 8
	v_or_b32_e32 v2, s3, v0
	s_addk_i32 s3, 0x100
	v_ashrrev_i32_e32 v3, 31, v2
	v_or_b32_e32 v4, s3, v0
	s_waitcnt lgkmcnt(0)
	v_lshl_add_u64 v[2:3], v[2:3], 2, s[6:7]
	v_ashrrev_i32_e32 v5, 31, v4
	v_lshl_add_u64 v[4:5], v[4:5], 2, s[6:7]
	global_load_dword v14, v[2:3], off
	global_load_dword v12, v[4:5], off

_Z6k_gemmPK15HIP_vector_typeIjLj4EES2_PKS_IjLj2EES5_PKfS7_S7_PjS8_:
	s_load_dwordx16 s[32:47], s[0:1], 0x0
	s_load_dwordx2 s[10:11], s[0:1], 0x40
	v_and_b32_e32 v4, 63, v0
	v_lshrrev_b32_e32 v94, 6, v0
	v_and_b32_e32 v1, 31, v0
	s_movk_i32 s3, 0xff
	v_cmp_lt_u32_e64 s[6:7], s3, v0
	s_movk_i32 s3, 0x100
	v_cmp_gt_u32_e64 s[4:5], s3, v0
	v_lshlrev_b32_e32 v98, 10, v94
	v_lshlrev_b32_e32 v5, 5, v4
	v_lshl_or_b32 v2, v94, 13, v5
	v_mov_b32_e32 v3, 0
	v_mov_b32_e32 v29, 0
	v_mov_b32_e32 v9, 0
	v_mov_b32_e32 v31, 0
	v_and_b32_e32 v8, 32, v4
	v_bfe_u32 v10, v0, 6, 1
	v_lshlrev_b32_e32 v30, 4, v10
	v_lshrrev_b32_e32 v5, 5, v0
	v_and_b32_e32 v5, 4, v5
	v_lshlrev_b32_e32 v28, 4, v5
	s_lshl_b32 s16, s2, 6
	s_lshl_b32 s17, s2, 1
	v_or_b32_e32 v5, s16, v1
	v_min_i32_e32 v5, 0xc34f, v5
	v_lshlrev_b32_e32 v6, 4, v5
	v_ashrrev_i32_e32 v7, 31, v6
	s_or_b32 s12, s17, 1
	s_min_i32 s12, s12, 0x61b
	v_lshl_or_b32 v5, s12, 5, v1
	v_min_i32_e32 v5, 0xc34f, v5
	v_lshlrev_b32_e32 v100, 4, v5
	v_ashrrev_i32_e32 v101, 31, v100
	v_readfirstlane_b32 s13, v98
	v_or_b32_e32 v5, 0x2000, v98
	s_movk_i32 s3, 0x200
	s_mov_b32 s18, 2
	s_nop 0
	s_mov_b32 s15, 0
	v_readfirstlane_b32 s19, v5
	s_waitcnt lgkmcnt(0)
	v_mov_b32_e32 v26, s38
	v_mov_b32_e32 v27, s39
	v_mov_b32_e32 v102, s36
	v_mov_b32_e32 v103, s37
	v_cndmask_b32_e64 v26, v26, v102, s[4:5]
	v_cndmask_b32_e64 v27, v27, v103, s[4:5]
	s_mov_b64 s[8:9], s[46:47]
	v_lshl_add_u64 v[6:7], v[6:7], 3, v[26:27]
	v_lshl_add_u64 v[100:101], v[100:101], 3, v[26:27]
	v_lshl_add_u64 v[6:7], v[6:7], 0, v[28:29]
	v_lshl_add_u64 v[100:101], v[100:101], 0, v[28:29]
	v_lshl_add_u64 v[6:7], v[6:7], 0, v[8:9]
	v_lshl_add_u64 v[100:101], v[100:101], 0, v[8:9]
	s_mov_b32 m0, s13
	v_lshl_add_u64 v[6:7], v[6:7], 0, v[30:31]
	v_lshl_add_u64 v[100:101], v[100:101], 0, v[30:31]
	global_load_lds_dwordx4 v[6:7], off
	global_load_dwordx4 v[34:37], v2, s[34:35]
	global_load_dwordx4 v[38:41], v2, s[34:35] offset:16
	s_mov_b32 m0, s19
	v_or_b32_e32 v5, 0x1000, v2
	global_load_lds_dwordx4 v[100:101], off
	global_load_dwordx4 v[50:53], v2, s[34:35] offset:2048
	global_load_dwordx4 v[54:57], v2, s[34:35] offset:2064
	global_load_dwordx4 v[66:69], v5, s[34:35]
	global_load_dwordx4 v[70:73], v5, s[34:35] offset:16
	global_load_dwordx4 v[42:45], v2, s[32:33]
	global_load_dwordx4 v[46:49], v2, s[32:33] offset:16
	global_load_dwordx4 v[58:61], v2, s[32:33] offset:2048
	global_load_dwordx4 v[62:65], v2, s[32:33] offset:2064
	global_load_dwordx4 v[74:77], v5, s[32:33]
	global_load_dwordx4 v[78:81], v5, s[32:33] offset:16
	global_load_dwordx4 v[82:85], v5, s[32:33] offset:2048
	global_load_dwordx4 v[86:89], v5, s[32:33] offset:2064
	v_lshlrev_b32_e32 v104, 1, v0
	v_lshrrev_b32_e32 v105, 2, v0
	v_and_b32_e32 v106, 0xe3, v0
	v_and_b32_e32 v104, 24, v104
	v_and_b32_e32 v105, 4, v105
	v_or3_b32 v106, v104, v106, v105
	v_lshlrev_b32_e32 v106, 2, v106
	v_mov_b32_e32 v107, 0x12300
	v_lshl_add_u32 v107, v0, 2, v107
	v_lshl_add_u64 v[2:3], s[34:35], 0, v[2:3]
	s_and_saveexec_b64 s[12:13], s[4:5]
	s_cbranch_execz .Lg_pro_nobias
	global_load_dword v108, v106, s[40:41]
	global_load_dword v109, v106, s[44:45]
	v_mov_b32_e32 v110, 0
	s_movk_i32 s0, 0x7f
	v_cmp_lt_u32_e32 vcc, s0, v0
	s_and_saveexec_b64 s[20:21], vcc
	s_cbranch_execz .Lg_pro_nob2
	global_load_dword v110, v106, s[42:43] offset:-512

.Lg_pro_nobias:
	s_or_b64 exec, exec, s[12:13]
	s_waitcnt vmcnt(0)
	s_sub_i32 s14, s18, s15
	s_cmp_lt_i32 s14, 1
	s_cbranch_scc1 .LBB2_40
	s_mov_b64 s[0:1], 0x1800
	v_lshl_add_u64 v[90:91], v[2:3], 0, s[0:1]
	s_movk_i32 s0, 0x1000
	v_add_co_u32_e32 v2, vcc, s0, v2
	s_waitcnt lgkmcnt(0)
	s_barrier
	s_nop 0
	v_addc_co_u32_e32 v3, vcc, 0, v3, vcc
	global_load_dwordx4 v[18:21], v[2:3], off offset:2048
	global_load_dwordx4 v[22:25], v[90:91], off offset:16
	v_lshrrev_b32_e32 v95, 5, v4
	v_mov_b32_e32 v5, 0x12300
	v_lshl_add_u32 v32, v94, 7, v5
	v_lshlrev_b32_e32 v33, 6, v95
	v_or_b32_e32 v14, v32, v33
	v_lshlrev_b32_e32 v99, 4, v4
	ds_read_b128 v[2:5], v14
	ds_read_b128 v[6:9], v14 offset:16
	ds_read_b128 v[10:13], v14 offset:32
	ds_read_b128 v[14:17], v14 offset:48
	s_nop 0
	ds_read_b128 v[100:103], v99
	ds_read_b128 v[104:107], v99 offset:1024
	v_mov_b32_e32 v96, 0x7f7f7f7f
	v_lshlrev_b32_e32 v92, 1, v95
	v_lshl_add_u64 v[26:27], v[26:27], 0, v[28:29]
	s_waitcnt lgkmcnt(0)
	v_mfma_scale_f32_32x32x64_f8f6f4 v[2:17], v[34:41], v[100:107], v[2:17], v96, v96 op_sel_hi:[0,0,0]
	v_lshlrev_b32_e32 v28, 4, v92
	s_cmpk_lt_i32 s2, 0x30d
	v_lshl_add_u64 v[26:27], v[26:27], 0, v[28:29]
	s_cselect_b64 s[0:1], -1, 0
	s_add_i32 s12, s2, 0x400
	v_lshl_add_u64 v[92:93], v[26:27], 0, v[30:31]
	v_lshl_or_b32 v26, s12, 5, v1
	v_min_i32_e32 v26, 0xc34f, v26
	s_add_i32 s13, s12, 0x200
	v_lshlrev_b32_e32 v26, 4, v26
	v_or_b32_e32 v28, 0x4000, v98
	s_cmpk_lt_i32 s2, 27
	v_ashrrev_i32_e32 v27, 31, v26
	v_readfirstlane_b32 s12, v28
	s_cselect_b32 s13, s13, 0x61b
	v_lshl_add_u64 v[26:27], v[26:27], 3, v[92:93]
	s_mov_b32 m0, s12
	ds_read_b128 v[100:103], v99 offset:2048
	ds_read_b128 v[104:107], v99 offset:3072
	global_load_lds_dwordx4 v[26:27], off
	v_lshl_or_b32 v26, s13, 5, v1
	v_min_i32_e32 v26, 0xc34f, v26
	v_lshlrev_b32_e32 v26, 4, v26
	v_or_b32_e32 v28, 0x6000, v98
	v_ashrrev_i32_e32 v27, 31, v26
	v_readfirstlane_b32 s12, v28
	v_lshl_add_u64 v[26:27], v[26:27], 3, v[92:93]
	s_mov_b32 m0, s12
	s_waitcnt lgkmcnt(0)
	v_mfma_scale_f32_32x32x64_f8f6f4 v[2:17], v[50:57], v[100:107], v[2:17], v96, v96 op_sel_hi:[0,0,0]
	s_nop 0
	ds_read_b128 v[100:103], v99 offset:4096
	ds_read_b128 v[104:107], v99 offset:5120
	global_load_lds_dwordx4 v[26:27], off
	v_mov_b32_e32 v26, v29
	s_cmpk_gt_i32 s2, 0x30c
	s_waitcnt lgkmcnt(0)
	v_mfma_scale_f32_32x32x64_f8f6f4 v[2:17], v[66:73], v[100:107], v[2:17], v96, v96 op_sel_hi:[0,0,0]
	s_waitcnt vmcnt(2)
	ds_read_b128 v[100:103], v99 offset:6144
	ds_read_b128 v[104:107], v99 offset:7168
	s_waitcnt lgkmcnt(0)
	v_mfma_scale_f32_32x32x64_f8f6f4 v[2:17], v[18:25], v[100:107], v[2:17], v96, v96 op_sel_hi:[0,0,0]
	s_nop 15
	s_nop 3
	v_mul_f32_e32 v2, 0xbfb8aa3b, v2
	v_mul_f32_e32 v3, 0xbfb8aa3b, v3
	v_exp_f32_e32 v2, v2
	v_exp_f32_e32 v3, v3
	v_mul_f32_e32 v4, 0xbfb8aa3b, v4
	v_mul_f32_e32 v5, 0xbfb8aa3b, v5
	v_exp_f32_e32 v4, v4
	v_exp_f32_e32 v5, v5
	v_add_f32_e32 v2, 1.0, v2
	v_add_f32_e32 v3, 1.0, v3
	v_rcp_f32_e32 v2, v2
	v_rcp_f32_e32 v3, v3
	v_add_f32_e32 v4, 1.0, v4
	v_add_f32_e32 v5, 1.0, v5
	v_rcp_f32_e32 v4, v4
	v_rcp_f32_e32 v5, v5
	v_add_f32_e32 v2, -0.5, v2
	v_add_f32_e32 v3, -0.5, v3
	v_cvt_pk_fp8_f32 v26, v2, v3
	v_add_f32_e32 v2, -0.5, v4
	v_add_f32_e32 v3, -0.5, v5
	v_cvt_pk_fp8_f32 v26, v2, v3 op_sel:[0,0,1]
	v_or_b32_e32 v2, 0x8000, v98
	v_add_u32_e32 v100, v2, v99
	v_mul_f32_e32 v2, 0xbfb8aa3b, v6
	v_mul_f32_e32 v3, 0xbfb8aa3b, v7
	v_exp_f32_e32 v2, v2
	v_exp_f32_e32 v3, v3
	v_mul_f32_e32 v4, 0xbfb8aa3b, v8
	v_mul_f32_e32 v5, 0xbfb8aa3b, v9
	v_add_f32_e32 v2, 1.0, v2
	v_exp_f32_e32 v4, v4
	v_add_f32_e32 v3, 1.0, v3
	v_exp_f32_e32 v5, v5
	v_rcp_f32_e32 v2, v2
	v_rcp_f32_e32 v3, v3
	v_add_f32_e32 v4, 1.0, v4
	v_add_f32_e32 v5, 1.0, v5
	v_add_f32_e32 v2, -0.5, v2
	v_add_f32_e32 v3, -0.5, v3
	v_rcp_f32_e32 v4, v4
	v_rcp_f32_e32 v5, v5
	v_mov_b32_e32 v27, v29
	v_cvt_pk_fp8_f32 v27, v2, v3
	v_add_f32_e32 v2, -0.5, v4
	v_add_f32_e32 v3, -0.5, v5
	v_cvt_pk_fp8_f32 v27, v2, v3 op_sel:[0,0,1]
	v_mul_f32_e32 v2, 0xbfb8aa3b, v10
	v_mul_f32_e32 v3, 0xbfb8aa3b, v11
	v_exp_f32_e32 v2, v2
	v_exp_f32_e32 v3, v3
	v_mul_f32_e32 v4, 0xbfb8aa3b, v12
	v_mul_f32_e32 v5, 0xbfb8aa3b, v13
	v_add_f32_e32 v2, 1.0, v2
	v_exp_f32_e32 v4, v4
	v_add_f32_e32 v3, 1.0, v3
	v_exp_f32_e32 v5, v5
	v_rcp_f32_e32 v2, v2
	v_rcp_f32_e32 v3, v3
	v_add_f32_e32 v4, 1.0, v4
	v_add_f32_e32 v5, 1.0, v5
	v_add_f32_e32 v2, -0.5, v2
	v_add_f32_e32 v3, -0.5, v3
	v_rcp_f32_e32 v4, v4
	v_rcp_f32_e32 v5, v5
	v_mov_b32_e32 v28, v29
	v_cvt_pk_fp8_f32 v28, v2, v3
	v_add_f32_e32 v2, -0.5, v4
	v_add_f32_e32 v3, -0.5, v5
	v_cvt_pk_fp8_f32 v28, v2, v3 op_sel:[0,0,1]
	v_mul_f32_e32 v2, 0xbfb8aa3b, v14
	v_mul_f32_e32 v3, 0xbfb8aa3b, v15
	v_exp_f32_e32 v2, v2
	v_exp_f32_e32 v3, v3
	v_mul_f32_e32 v4, 0xbfb8aa3b, v16
	v_mul_f32_e32 v5, 0xbfb8aa3b, v17
	v_add_f32_e32 v2, 1.0, v2
	v_exp_f32_e32 v4, v4
	v_add_f32_e32 v3, 1.0, v3
	v_exp_f32_e32 v5, v5
	v_rcp_f32_e32 v2, v2
	v_rcp_f32_e32 v3, v3
	v_add_f32_e32 v4, 1.0, v4
	v_add_f32_e32 v5, 1.0, v5
	v_add_f32_e32 v2, -0.5, v2
	v_add_f32_e32 v3, -0.5, v3
	v_rcp_f32_e32 v4, v4
	v_rcp_f32_e32 v5, v5
	v_cvt_pk_fp8_f32 v29, v2, v3
	v_add_f32_e32 v2, -0.5, v4
	v_add_f32_e32 v3, -0.5, v5
	v_cvt_pk_fp8_f32 v29, v2, v3 op_sel:[0,0,1]
	v_add_u32_e32 v101, v32, v33
	ds_write_b128 v100, v[26:29]
	s_cbranch_scc1 .LBB2_7
	ds_read_b128 v[2:5], v101
	ds_read_b128 v[6:9], v101 offset:16
	ds_read_b128 v[10:13], v101 offset:32
	ds_read_b128 v[14:17], v101 offset:48
	ds_read_b128 v[26:29], v99 offset:8192
	ds_read_b128 v[30:33], v99 offset:9216
	s_waitcnt lgkmcnt(0)
	v_mfma_scale_f32_32x32x64_f8f6f4 v[2:17], v[34:41], v[26:33], v[2:17], v96, v96 op_sel_hi:[0,0,0]
	ds_read_b128 v[26:29], v99 offset:10240
	ds_read_b128 v[30:33], v99 offset:11264
	s_waitcnt lgkmcnt(0)
	v_mfma_scale_f32_32x32x64_f8f6f4 v[2:17], v[50:57], v[26:33], v[2:17], v96, v96 op_sel_hi:[0,0,0]
	ds_read_b128 v[26:29], v99 offset:12288
	ds_read_b128 v[30:33], v99 offset:13312
	s_waitcnt lgkmcnt(0)
	v_mfma_scale_f32_32x32x64_f8f6f4 v[2:17], v[66:73], v[26:33], v[2:17], v96, v96 op_sel_hi:[0,0,0]
	ds_read_b128 v[26:29], v99 offset:14336
	ds_read_b128 v[30:33], v99 offset:15360
	s_waitcnt lgkmcnt(0)
	v_mfma_scale_f32_32x32x64_f8f6f4 v[2:17], v[18:25], v[26:33], v[2:17], v96, v96 op_sel_hi:[0,0,0]
	s_nop 15
	s_nop 3
	v_mul_f32_e32 v2, 0xbfb8aa3b, v2
	v_mul_f32_e32 v3, 0xbfb8aa3b, v3
	v_exp_f32_e32 v2, v2
	v_exp_f32_e32 v3, v3
	v_mul_f32_e32 v4, 0xbfb8aa3b, v4
	v_mul_f32_e32 v5, 0xbfb8aa3b, v5
	v_exp_f32_e32 v4, v4
	v_exp_f32_e32 v5, v5
	v_add_f32_e32 v2, 1.0, v2
	v_add_f32_e32 v3, 1.0, v3
	v_rcp_f32_e32 v2, v2
	v_rcp_f32_e32 v3, v3
	v_add_f32_e32 v4, 1.0, v4
	v_add_f32_e32 v5, 1.0, v5
	v_rcp_f32_e32 v4, v4
	v_rcp_f32_e32 v5, v5
	v_add_f32_e32 v18, -0.5, v2
	v_add_f32_e32 v3, -0.5, v3
	v_mov_b32_e32 v2, 0
	v_cvt_pk_fp8_f32 v2, v18, v3
	v_add_f32_e32 v3, -0.5, v4
	v_add_f32_e32 v4, -0.5, v5
	v_mov_b32_e32 v5, 0
	v_cvt_pk_fp8_f32 v2, v3, v4 op_sel:[0,0,1]
	v_mul_f32_e32 v3, 0xbfb8aa3b, v6
	v_exp_f32_e32 v3, v3
	v_mul_f32_e32 v4, 0xbfb8aa3b, v7
	v_exp_f32_e32 v4, v4
	v_mul_f32_e32 v6, 0xbfb8aa3b, v8
	v_add_f32_e32 v3, 1.0, v3
	v_rcp_f32_e32 v3, v3
	v_exp_f32_e32 v6, v6
	v_add_f32_e32 v4, 1.0, v4
	v_rcp_f32_e32 v4, v4
	v_add_f32_e32 v7, -0.5, v3
	v_mul_f32_e32 v3, 0xbfb8aa3b, v9
	v_exp_f32_e32 v3, v3
	v_add_f32_e32 v6, 1.0, v6
	v_add_f32_e32 v4, -0.5, v4
	v_rcp_f32_e32 v6, v6
	v_add_f32_e32 v3, 1.0, v3
	v_rcp_f32_e32 v8, v3
	v_mov_b32_e32 v3, 0
	v_cvt_pk_fp8_f32 v3, v7, v4
	v_add_f32_e32 v4, -0.5, v6
	v_add_f32_e32 v6, -0.5, v8
	v_cvt_pk_fp8_f32 v3, v4, v6 op_sel:[0,0,1]
	v_mul_f32_e32 v4, 0xbfb8aa3b, v10
	v_exp_f32_e32 v4, v4
	v_mul_f32_e32 v6, 0xbfb8aa3b, v11
	v_exp_f32_e32 v6, v6
	v_mul_f32_e32 v7, 0xbfb8aa3b, v12
	v_add_f32_e32 v4, 1.0, v4
	v_rcp_f32_e32 v4, v4
	v_exp_f32_e32 v7, v7
	v_add_f32_e32 v6, 1.0, v6
	v_rcp_f32_e32 v6, v6
	v_add_f32_e32 v8, -0.5, v4
	v_mul_f32_e32 v4, 0xbfb8aa3b, v13
	v_exp_f32_e32 v4, v4
	v_add_f32_e32 v7, 1.0, v7
	v_add_f32_e32 v6, -0.5, v6
	v_rcp_f32_e32 v7, v7
	v_add_f32_e32 v4, 1.0, v4
	v_rcp_f32_e32 v9, v4
	v_mov_b32_e32 v4, 0
	v_cvt_pk_fp8_f32 v4, v8, v6
	v_add_f32_e32 v6, -0.5, v7
	v_add_f32_e32 v7, -0.5, v9
	v_cvt_pk_fp8_f32 v4, v6, v7 op_sel:[0,0,1]
	v_mul_f32_e32 v6, 0xbfb8aa3b, v14
	v_mul_f32_e32 v7, 0xbfb8aa3b, v15
	v_exp_f32_e32 v6, v6
	v_exp_f32_e32 v7, v7
	v_mul_f32_e32 v8, 0xbfb8aa3b, v16
	v_mul_f32_e32 v9, 0xbfb8aa3b, v17
	v_add_f32_e32 v6, 1.0, v6
	v_exp_f32_e32 v8, v8
	v_add_f32_e32 v7, 1.0, v7
	v_exp_f32_e32 v9, v9
	v_rcp_f32_e32 v6, v6
	v_rcp_f32_e32 v7, v7
	v_add_f32_e32 v8, 1.0, v8
	v_add_f32_e32 v9, 1.0, v9
	v_add_f32_e32 v6, -0.5, v6
	v_add_f32_e32 v7, -0.5, v7
	v_rcp_f32_e32 v8, v8
	v_rcp_f32_e32 v9, v9
	v_cvt_pk_fp8_f32 v5, v6, v7
	v_add_f32_e32 v6, -0.5, v8
	v_add_f32_e32 v7, -0.5, v9
	v_cvt_pk_fp8_f32 v5, v6, v7 op_sel:[0,0,1]
	ds_write_b128 v100, v[2:5] offset:8192

.LBB2_29:
	s_cmpk_lt_i32 s2, 27
	s_cselect_b32 s23, 0, 0x30d
	s_cmpk_lt_i32 s23, 0x30d
	s_cselect_b64 s[0:1], -1, 0
	s_xor_b32 s24, s12, 1
	v_min_i32_e32 v2, 0xc34f, v107
	v_lshlrev_b32_e32 v2, 4, v2
	v_lshl_or_b32 v4, s24, 14, v98
	s_add_i32 s13, s18, s17
	v_ashrrev_i32_e32 v3, 31, v2
	v_readfirstlane_b32 s25, v4
	s_min_i32 s13, s13, 0x61b
	v_lshl_add_u64 v[2:3], v[2:3], 3, v[92:93]
	s_mov_b32 m0, s25
	v_or_b32_e32 v4, 0x2000, v4
	global_load_lds_dwordx4 v[2:3], off
	v_lshl_or_b32 v2, s13, 5, v1
	v_min_i32_e32 v2, 0xc34f, v2
	v_lshlrev_b32_e32 v2, 4, v2
	v_ashrrev_i32_e32 v3, 31, v2
	v_readfirstlane_b32 s13, v4
	s_lshl_b32 s12, s12, 14
	v_lshl_add_u64 v[2:3], v[2:3], 3, v[92:93]
	s_mov_b32 m0, s13
	v_or_b32_e32 v95, s12, v99
	global_load_lds_dwordx4 v[2:3], off
	ds_read_b128 v[2:5], v101
	ds_read_b128 v[6:9], v101 offset:16
	ds_read_b128 v[10:13], v101 offset:32
	ds_read_b128 v[14:17], v101 offset:48
	s_nop 0
	ds_read_b128 v[26:29], v95
	ds_read_b128 v[30:33], v95 offset:1024
	s_waitcnt lgkmcnt(0)
	v_mfma_scale_f32_32x32x64_f8f6f4 v[2:17], v[34:41], v[26:33], v[2:17], v110, v110 op_sel_hi:[0,0,0]
	ds_read_b128 v[26:29], v95 offset:2048
	ds_read_b128 v[30:33], v95 offset:3072
	s_cmpk_gt_i32 s23, 0x30c
	s_waitcnt lgkmcnt(0)
	v_mfma_scale_f32_32x32x64_f8f6f4 v[2:17], v[50:57], v[26:33], v[2:17], v110, v110 op_sel_hi:[0,0,0]
	ds_read_b128 v[26:29], v95 offset:4096
	ds_read_b128 v[30:33], v95 offset:5120
	s_waitcnt lgkmcnt(0)
	v_mfma_scale_f32_32x32x64_f8f6f4 v[2:17], v[66:73], v[26:33], v[2:17], v110, v110 op_sel_hi:[0,0,0]
	ds_read_b128 v[26:29], v95 offset:6144
	ds_read_b128 v[30:33], v95 offset:7168
	s_waitcnt lgkmcnt(0)
	s_waitcnt vmcnt(2)
	v_mfma_scale_f32_32x32x64_f8f6f4 v[2:17], v[18:25], v[26:33], v[2:17], v110, v110 op_sel_hi:[0,0,0]
	s_nop 15
	s_nop 3
	v_mul_f32_e32 v2, 0xbfb8aa3b, v2
	v_mul_f32_e32 v3, 0xbfb8aa3b, v3
	v_exp_f32_e32 v2, v2
	v_exp_f32_e32 v3, v3
	v_mul_f32_e32 v4, 0xbfb8aa3b, v4
	v_mul_f32_e32 v5, 0xbfb8aa3b, v5
	v_exp_f32_e32 v4, v4
	v_exp_f32_e32 v5, v5
	v_add_f32_e32 v2, 1.0, v2
	v_add_f32_e32 v3, 1.0, v3
	v_rcp_f32_e32 v2, v2
	v_rcp_f32_e32 v3, v3
	v_add_f32_e32 v4, 1.0, v4
	v_add_f32_e32 v5, 1.0, v5
	v_rcp_f32_e32 v4, v4
	v_rcp_f32_e32 v5, v5
	v_add_f32_e32 v26, -0.5, v2
	v_add_f32_e32 v3, -0.5, v3
	v_mov_b32_e32 v2, 0
	v_cvt_pk_fp8_f32 v2, v26, v3
	v_add_f32_e32 v3, -0.5, v4
	v_add_f32_e32 v4, -0.5, v5
	v_cvt_pk_fp8_f32 v2, v3, v4 op_sel:[0,0,1]
	v_mul_f32_e32 v3, 0xbfb8aa3b, v6
	v_exp_f32_e32 v3, v3
	v_mul_f32_e32 v4, 0xbfb8aa3b, v7
	v_exp_f32_e32 v4, v4
	v_mul_f32_e32 v5, 0xbfb8aa3b, v8
	v_add_f32_e32 v3, 1.0, v3
	v_rcp_f32_e32 v3, v3
	v_exp_f32_e32 v5, v5
	v_add_f32_e32 v4, 1.0, v4
	v_rcp_f32_e32 v4, v4
	v_add_f32_e32 v6, -0.5, v3
	v_mul_f32_e32 v3, 0xbfb8aa3b, v9
	v_exp_f32_e32 v3, v3
	v_add_f32_e32 v5, 1.0, v5
	v_add_f32_e32 v4, -0.5, v4
	v_rcp_f32_e32 v5, v5
	v_add_f32_e32 v3, 1.0, v3
	v_rcp_f32_e32 v7, v3
	v_mov_b32_e32 v3, 0
	v_cvt_pk_fp8_f32 v3, v6, v4
	v_add_f32_e32 v4, -0.5, v5
	v_add_f32_e32 v5, -0.5, v7
	v_cvt_pk_fp8_f32 v3, v4, v5 op_sel:[0,0,1]
	v_mul_f32_e32 v4, 0xbfb8aa3b, v10
	v_exp_f32_e32 v4, v4
	v_mul_f32_e32 v5, 0xbfb8aa3b, v11
	v_exp_f32_e32 v5, v5
	v_mul_f32_e32 v6, 0xbfb8aa3b, v12
	v_add_f32_e32 v4, 1.0, v4
	v_rcp_f32_e32 v4, v4
	v_exp_f32_e32 v6, v6
	v_add_f32_e32 v5, 1.0, v5
	v_rcp_f32_e32 v5, v5
	v_add_f32_e32 v7, -0.5, v4
	v_mul_f32_e32 v4, 0xbfb8aa3b, v13
	v_exp_f32_e32 v4, v4
	v_add_f32_e32 v6, 1.0, v6
	v_add_f32_e32 v5, -0.5, v5
	v_rcp_f32_e32 v6, v6
	v_add_f32_e32 v4, 1.0, v4
	v_rcp_f32_e32 v8, v4
	v_mov_b32_e32 v4, 0
	v_cvt_pk_fp8_f32 v4, v7, v5
	v_add_f32_e32 v5, -0.5, v6
	v_add_f32_e32 v6, -0.5, v8
	v_cvt_pk_fp8_f32 v4, v5, v6 op_sel:[0,0,1]
	v_mul_f32_e32 v5, 0xbfb8aa3b, v14
	v_exp_f32_e32 v5, v5
	v_mul_f32_e32 v6, 0xbfb8aa3b, v15
	v_exp_f32_e32 v6, v6
	v_mul_f32_e32 v7, 0xbfb8aa3b, v16
	v_add_f32_e32 v5, 1.0, v5
	v_rcp_f32_e32 v5, v5
	v_exp_f32_e32 v7, v7
	v_add_f32_e32 v6, 1.0, v6
	v_rcp_f32_e32 v6, v6
	v_add_f32_e32 v8, -0.5, v5
	v_mul_f32_e32 v5, 0xbfb8aa3b, v17
	v_exp_f32_e32 v5, v5
	v_add_f32_e32 v7, 1.0, v7
	v_add_f32_e32 v6, -0.5, v6
	v_rcp_f32_e32 v7, v7
	v_add_f32_e32 v5, 1.0, v5
	v_rcp_f32_e32 v9, v5
	v_mov_b32_e32 v5, 0
	v_cvt_pk_fp8_f32 v5, v8, v6
	v_add_f32_e32 v6, -0.5, v7
	v_add_f32_e32 v7, -0.5, v9
	v_cvt_pk_fp8_f32 v5, v6, v7 op_sel:[0,0,1]
	ds_write_b128 v100, v[2:5]
	s_cbranch_scc1 .LBB2_31
	v_add_u32_e32 v95, s12, v99
	ds_read_b128 v[2:5], v101
	ds_read_b128 v[6:9], v101 offset:16
	ds_read_b128 v[10:13], v101 offset:32
	ds_read_b128 v[14:17], v101 offset:48
	ds_read_b128 v[26:29], v95 offset:8192
	ds_read_b128 v[30:33], v95 offset:9216
	s_waitcnt lgkmcnt(0)
	v_mfma_scale_f32_32x32x64_f8f6f4 v[2:17], v[34:41], v[26:33], v[2:17], v110, v110 op_sel_hi:[0,0,0]
	ds_read_b128 v[26:29], v95 offset:10240
	ds_read_b128 v[30:33], v95 offset:11264
	s_waitcnt lgkmcnt(0)
	v_mfma_scale_f32_32x32x64_f8f6f4 v[2:17], v[50:57], v[26:33], v[2:17], v110, v110 op_sel_hi:[0,0,0]
	ds_read_b128 v[26:29], v95 offset:12288
	ds_read_b128 v[30:33], v95 offset:13312
	s_waitcnt lgkmcnt(0)
	v_mfma_scale_f32_32x32x64_f8f6f4 v[2:17], v[66:73], v[26:33], v[2:17], v110, v110 op_sel_hi:[0,0,0]
	ds_read_b128 v[26:29], v95 offset:14336
	ds_read_b128 v[30:33], v95 offset:15360
	s_waitcnt lgkmcnt(0)
	v_mfma_scale_f32_32x32x64_f8f6f4 v[2:17], v[18:25], v[26:33], v[2:17], v110, v110 op_sel_hi:[0,0,0]
	s_nop 15
	s_nop 3
	v_mul_f32_e32 v2, 0xbfb8aa3b, v2
	v_mul_f32_e32 v3, 0xbfb8aa3b, v3
	v_exp_f32_e32 v2, v2
	v_exp_f32_e32 v3, v3
	v_mul_f32_e32 v4, 0xbfb8aa3b, v4
	v_mul_f32_e32 v5, 0xbfb8aa3b, v5
	v_exp_f32_e32 v4, v4
	v_exp_f32_e32 v5, v5
	v_add_f32_e32 v2, 1.0, v2
	v_add_f32_e32 v3, 1.0, v3
	v_rcp_f32_e32 v2, v2
	v_rcp_f32_e32 v3, v3
	v_add_f32_e32 v4, 1.0, v4
	v_add_f32_e32 v5, 1.0, v5
	v_rcp_f32_e32 v4, v4
	v_rcp_f32_e32 v5, v5
	v_add_f32_e32 v18, -0.5, v2
	v_add_f32_e32 v3, -0.5, v3
	v_mov_b32_e32 v2, 0
	v_cvt_pk_fp8_f32 v2, v18, v3
	v_add_f32_e32 v3, -0.5, v4
	v_add_f32_e32 v4, -0.5, v5
	v_cvt_pk_fp8_f32 v2, v3, v4 op_sel:[0,0,1]
	v_mul_f32_e32 v3, 0xbfb8aa3b, v6
	v_exp_f32_e32 v3, v3
	v_mul_f32_e32 v4, 0xbfb8aa3b, v7
	v_exp_f32_e32 v4, v4
	v_mul_f32_e32 v5, 0xbfb8aa3b, v8
	v_add_f32_e32 v3, 1.0, v3
	v_rcp_f32_e32 v3, v3
	v_exp_f32_e32 v5, v5
	v_add_f32_e32 v4, 1.0, v4
	v_rcp_f32_e32 v4, v4
	v_add_f32_e32 v6, -0.5, v3
	v_mul_f32_e32 v3, 0xbfb8aa3b, v9
	v_exp_f32_e32 v3, v3
	v_add_f32_e32 v5, 1.0, v5
	v_add_f32_e32 v4, -0.5, v4
	v_rcp_f32_e32 v5, v5
	v_add_f32_e32 v3, 1.0, v3
	v_rcp_f32_e32 v7, v3
	v_mov_b32_e32 v3, 0
	v_cvt_pk_fp8_f32 v3, v6, v4
	v_add_f32_e32 v4, -0.5, v5
	v_add_f32_e32 v5, -0.5, v7
	v_cvt_pk_fp8_f32 v3, v4, v5 op_sel:[0,0,1]
	v_mul_f32_e32 v4, 0xbfb8aa3b, v10
	v_exp_f32_e32 v4, v4
	v_mul_f32_e32 v5, 0xbfb8aa3b, v11
	v_exp_f32_e32 v5, v5
	v_mul_f32_e32 v6, 0xbfb8aa3b, v12
	v_add_f32_e32 v4, 1.0, v4
	v_rcp_f32_e32 v4, v4
	v_exp_f32_e32 v6, v6
	v_add_f32_e32 v5, 1.0, v5
	v_rcp_f32_e32 v5, v5
	v_add_f32_e32 v7, -0.5, v4
	v_mul_f32_e32 v4, 0xbfb8aa3b, v13
	v_exp_f32_e32 v4, v4
	v_add_f32_e32 v6, 1.0, v6
	v_add_f32_e32 v5, -0.5, v5
	v_rcp_f32_e32 v6, v6
	v_add_f32_e32 v4, 1.0, v4
	v_rcp_f32_e32 v8, v4
	v_mov_b32_e32 v4, 0
	v_cvt_pk_fp8_f32 v4, v7, v5
	v_add_f32_e32 v5, -0.5, v6
	v_add_f32_e32 v6, -0.5, v8
	v_cvt_pk_fp8_f32 v4, v5, v6 op_sel:[0,0,1]
	v_mul_f32_e32 v5, 0xbfb8aa3b, v14
	v_exp_f32_e32 v5, v5
	v_mul_f32_e32 v6, 0xbfb8aa3b, v15
	v_exp_f32_e32 v6, v6
	v_mul_f32_e32 v7, 0xbfb8aa3b, v16
	v_add_f32_e32 v5, 1.0, v5
	v_rcp_f32_e32 v5, v5
	v_exp_f32_e32 v7, v7
	v_add_f32_e32 v6, 1.0, v6
	v_rcp_f32_e32 v6, v6
	v_add_f32_e32 v8, -0.5, v5
	v_mul_f32_e32 v5, 0xbfb8aa3b, v17
	v_exp_f32_e32 v5, v5
	v_add_f32_e32 v7, 1.0, v7
	v_add_f32_e32 v6, -0.5, v6
	v_rcp_f32_e32 v7, v7
	v_add_f32_e32 v5, 1.0, v5
	v_rcp_f32_e32 v9, v5
	v_mov_b32_e32 v5, 0
	v_cvt_pk_fp8_f32 v5, v8, v6
	v_add_f32_e32 v6, -0.5, v7
	v_add_f32_e32 v7, -0.5, v9
	v_cvt_pk_fp8_f32 v5, v6, v7 op_sel:[0,0,1]
	ds_write_b128 v100, v[2:5] offset:8192

.LBB2_40:
	s_add_i32 s0, s14, -1
	s_waitcnt lgkmcnt(0)
	s_nop 0
	s_nop 0
	s_cmpk_gt_i32 s2, 0x30d
	v_lshrrev_b32_e32 v1, 4, v0
	s_nop 6
	v_and_b32_e32 v2, 15, v0
	s_barrier
	s_cbranch_scc0 .LBB2_43
	s_lshl_b32 s0, s2, 1
	s_or_b32 s0, s0, 1
	s_cmpk_gt_i32 s0, 0x61a
	s_cbranch_scc0 .LBB2_46

.LBB2_43:
	s_addk_i32 s2, 0x400
	v_mul_u32_u24_e32 v3, 0x108, v1
	v_lshlrev_b32_e32 v4, 4, v2
	s_mov_b32 s0, 0xc000
	v_add3_u32 v3, v4, v3, s0
	s_lshl_b32 s3, s2, 5
	ds_read2_b64 v[4:7], v3 offset1:1
	v_or_b32_e32 v3, s3, v1
	v_lshl_or_b32 v8, v3, 4, v2
	v_ashrrev_i32_e32 v9, 31, v8
	v_lshl_add_u64 v[8:9], v[8:9], 4, s[10:11]
	s_waitcnt lgkmcnt(0)
	global_store_dwordx4 v[8:9], v[4:7], off
	s_and_saveexec_b64 s[0:1], s[4:5]
	s_cbranch_execz .LBB2_45
	v_lshrrev_b32_e32 v3, 3, v0
	v_and_b32_e32 v8, 7, v0
	v_mul_u32_u24_e32 v4, 0x84, v3
	v_lshlrev_b32_e32 v5, 4, v8
	s_mov_b32 s6, 0x10200
	v_add3_u32 v6, v4, v5, s6
	ds_read2_b32 v[4:5], v6 offset1:1
	ds_read2_b32 v[6:7], v6 offset0:2 offset1:3
	v_or_b32_e32 v3, s3, v3
	v_lshl_or_b32 v8, v3, 3, v8
	v_ashrrev_i32_e32 v9, 31, v8
	v_lshl_add_u64 v[8:9], v[8:9], 4, s[8:9]
	s_waitcnt lgkmcnt(0)
	global_store_dwordx4 v[8:9], v[4:7], off
.LBB2_45:
	s_or_b64 exec, exec, s[0:1]
	s_add_i32 s0, s2, 0x200
	s_cmpk_lt_i32 s2, 0x41b
	s_cselect_b32 s0, s0, 0x61b
	s_cmpk_gt_i32 s0, 0x61a
	s_cbranch_scc1 .LBB2_42
